# mLSTM gate GEMV tasks spread over all 256 workgroups (4 waves each) instead of 128 workgroups
# speedup vs baseline: 1.0041x; 1.0041x over previous
; __device__ __forceinline__ int fresh_lane() { unsigned z = 0u; asm volatile("" : "+v"(z)); return (int)__builtin_amdgcn_mbcnt_hi(~0u, __builtin_amdgcn_mbcnt_lo(~0u, z)); }
; __device__ __forceinline__ void ph_mlstm_gates(const Frame& F, int j) {
;     const bf16* XB = (const bf16*)(F.ws + WS_XB); const bf16* WGB = (const bf16*)(F.ws + WS_WGB) + (size_t)j * 16 * 2048; float* GA = (float*)(F.ws + WS_GA);
;     const int lane = fresh_lane(), l15 = lane & 15, g = lane >> 4;
;     for (int task = F.gw; task < T / 16; task += F.ngw) {
;         const bf16* xa = XB + (size_t)(task * 16 + l15) * D + 8 * g;
;         const bf16* wb = WGB + (size_t)l15 * 2048 + 8 * g;
;         f32x4 a0 = (f32x4){0.f, 0.f, 0.f, 0.f}, a1 = a0;
.LBB0_310:
	s_andn2_b64 vcc, exec, s[2:3]
	v_readlane_b32 s43, v254, 62
	s_cbranch_vccnz .LBB0_316
	v_readlane_b32 s0, v254, 55
	s_cmpk_gt_i32 s0, 3
	v_mov_b32_e32 v0, v1
	v_readlane_b32 s1, v254, 59
	s_cbranch_scc1 .LBB0_316
	v_readlane_b32 s0, v254, 60
	v_mbcnt_lo_u32_b32 v0, -1, v0
	v_readlane_b32 s1, v254, 61
	v_mbcnt_hi_u32_b32 v0, -1, v0
	s_mov_b32 s4, s0
	s_ashr_i32 s5, s0, 31
	v_writelane_b32 v254, s0, 60
	v_ashrrev_i32_e32 v4, 4, v0
	v_and_b32_e32 v6, 15, v0
	v_writelane_b32 v254, s1, 61
	s_lshl_b64 s[0:1], s[4:5], 16
	v_lshlrev_b32_e32 v2, 3, v4
	s_add_u32 s0, s60, s0
	v_ashrrev_i32_e32 v3, 31, v2
	v_lshlrev_b32_e32 v0, 12, v6
	s_addc_u32 s1, s61, s1
	v_lshlrev_b64 v[12:13], 1, v[2:3]
	v_lshl_add_u64 v[2:3], s[0:1], 0, v[0:1]
	s_mov_b64 s[0:1], 0xc580100
	v_lshlrev_b32_e32 v22, 2, v4
	v_lshlrev_b32_e32 v4, 2, v6
	v_mov_b32_e32 v5, v1
	v_lshl_add_u64 v[14:15], v[2:3], 0, s[0:1]
	v_readlane_b32 s1, v254, 55
	v_lshl_add_u64 v[4:5], s[60:61], 0, v[4:5]
	s_mov_b64 s[4:5], 0x73800000
	s_lshl_b32 s0, s44, 6
	s_lshl_b32 s1, s1, 4
	v_lshl_add_u64 v[10:11], v[4:5], 0, s[4:5]
	s_add_i32 s0, s0, s1
	s_lshr_b32 s4, s1, 4
	s_lshl_b32 s98, s44, 2
	s_add_i32 s4, s4, s98
	v_or_b32_e32 v16, s0, v6
	s_lshl_b32 s0, s45, 6
	s_mov_b32 s1, s4
	v_readlane_b32 s5, v254, 59

; __device__ __forceinline__ void ph_mlstm_gates(const Frame& F, int j) {
;     ...
; #pragma unroll 4
;         for (int st = 0; st < 64; st += 2) {
;             a0 = __builtin_amdgcn_mfma_f32_16x16x32_bf16(*(const bf16x8*)(xa + 32 * st), *(const bf16x8*)(wb + 32 * st), a0, 0, 0, 0);
;             a1 = __builtin_amdgcn_mfma_f32_16x16x32_bf16(*(const bf16x8*)(xa + 32 * st + 32), *(const bf16x8*)(wb + 32 * st + 32), a1, 0, 0, 0);
;         }
; #pragma unroll
;         for (int i = 0; i < 4; ++i) GA[(size_t)(task * 16 + 4 * g + i) * 16 + l15] = a0[i] + a1[i];
;     }
.Lgt_loop:
	global_load_dwordx4 v[104:107], v[32:33], off offset:512
	global_load_dwordx4 v[212:215], v[34:35], off offset:256
	global_load_dwordx4 v[108:111], v[32:33], off offset:576
	global_load_dwordx4 v[216:219], v[34:35], off offset:320
	global_load_dwordx4 v[112:115], v[32:33], off offset:640
	global_load_dwordx4 v[220:223], v[34:35], off offset:384
	global_load_dwordx4 v[116:119], v[32:33], off offset:704
	global_load_dwordx4 v[224:227], v[34:35], off offset:448
	global_load_dwordx4 v[120:123], v[32:33], off offset:768
	global_load_dwordx4 v[228:231], v[34:35], off offset:512
	global_load_dwordx4 v[124:127], v[32:33], off offset:832
	global_load_dwordx4 v[232:235], v[34:35], off offset:576
	global_load_dwordx4 v[128:131], v[32:33], off offset:896
	global_load_dwordx4 v[236:239], v[34:35], off offset:640
	global_load_dwordx4 v[132:135], v[32:33], off offset:960
	global_load_dwordx4 v[240:243], v[34:35], off offset:704
	s_waitcnt vmcnt(30)
	v_mfma_f32_16x16x32_bf16 v[2:5], v[40:43], v[72:75], v[2:5]
	s_waitcnt vmcnt(28)
	v_mfma_f32_16x16x32_bf16 v[6:9], v[44:47], v[76:79], v[6:9]
	s_waitcnt vmcnt(26)
	v_mfma_f32_16x16x32_bf16 v[2:5], v[48:51], v[80:83], v[2:5]
	s_waitcnt vmcnt(24)
	v_mfma_f32_16x16x32_bf16 v[6:9], v[52:55], v[84:87], v[6:9]
	s_waitcnt vmcnt(22)
	v_mfma_f32_16x16x32_bf16 v[2:5], v[56:59], v[88:91], v[2:5]
	s_waitcnt vmcnt(20)
	v_mfma_f32_16x16x32_bf16 v[6:9], v[60:63], v[92:95], v[6:9]
	s_waitcnt vmcnt(18)
	v_mfma_f32_16x16x32_bf16 v[2:5], v[64:67], v[96:99], v[2:5]
	s_waitcnt vmcnt(16)
	v_mfma_f32_16x16x32_bf16 v[6:9], v[68:71], v[100:103], v[6:9]
	global_load_dwordx4 v[40:43], v[32:33], off offset:1024
	global_load_dwordx4 v[72:75], v[34:35], off offset:768
	global_load_dwordx4 v[44:47], v[32:33], off offset:1088
	global_load_dwordx4 v[76:79], v[34:35], off offset:832
	global_load_dwordx4 v[48:51], v[32:33], off offset:1152
	global_load_dwordx4 v[80:83], v[34:35], off offset:896
	global_load_dwordx4 v[52:55], v[32:33], off offset:1216
	global_load_dwordx4 v[84:87], v[34:35], off offset:960
	global_load_dwordx4 v[56:59], v[32:33], off offset:1280
	global_load_dwordx4 v[88:91], v[34:35], off offset:1024
	global_load_dwordx4 v[60:63], v[32:33], off offset:1344
	global_load_dwordx4 v[92:95], v[34:35], off offset:1088
	global_load_dwordx4 v[64:67], v[32:33], off offset:1408
	global_load_dwordx4 v[96:99], v[34:35], off offset:1152
	global_load_dwordx4 v[68:71], v[32:33], off offset:1472
	global_load_dwordx4 v[100:103], v[34:35], off offset:1216
	s_waitcnt vmcnt(30)
	v_mfma_f32_16x16x32_bf16 v[2:5], v[104:107], v[212:215], v[2:5]
	s_waitcnt vmcnt(28)
	v_mfma_f32_16x16x32_bf16 v[6:9], v[108:111], v[216:219], v[6:9]
	s_waitcnt vmcnt(26)
	v_mfma_f32_16x16x32_bf16 v[2:5], v[112:115], v[220:223], v[2:5]
	s_waitcnt vmcnt(24)
	v_mfma_f32_16x16x32_bf16 v[6:9], v[116:119], v[224:227], v[6:9]
	s_waitcnt vmcnt(22)
	v_mfma_f32_16x16x32_bf16 v[2:5], v[120:123], v[228:231], v[2:5]
	s_waitcnt vmcnt(20)
	v_mfma_f32_16x16x32_bf16 v[6:9], v[124:127], v[232:235], v[6:9]
	s_waitcnt vmcnt(18)
	v_mfma_f32_16x16x32_bf16 v[2:5], v[128:131], v[236:239], v[2:5]
	s_waitcnt vmcnt(16)
	v_mfma_f32_16x16x32_bf16 v[6:9], v[132:135], v[240:243], v[6:9]
	v_lshl_add_u64 v[32:33], s[96:97], 1, v[32:33]
	v_lshl_add_u64 v[34:35], s[96:97], 1, v[34:35]
	s_add_i32 s4, s4, 1
	s_cmp_lt_u32 s4, 4
	s_cbranch_scc1 .Lgt_loop
	s_waitcnt vmcnt(0)
	v_lshl_add_u32 v18, s1, 4, v22
	v_ashrrev_i32_e32 v19, 31, v18
	v_lshlrev_b64 v[20:21], 6, v[18:19]
	s_nop 3
	v_add_f32_e32 v0, v2, v6
	v_lshl_add_u64 v[20:21], v[10:11], 0, v[20:21]
	v_or_b32_e32 v2, 1, v18
	global_store_dword v[20:21], v0, off
	v_add_f32_e32 v0, v3, v7
	v_ashrrev_i32_e32 v3, 31, v2
	v_lshlrev_b64 v[2:3], 6, v[2:3]
	v_lshl_add_u64 v[2:3], v[10:11], 0, v[2:3]
	global_store_dword v[2:3], v0, off
	v_or_b32_e32 v2, 2, v18
	v_ashrrev_i32_e32 v3, 31, v2
	v_lshlrev_b64 v[2:3], 6, v[2:3]
	v_add_f32_e32 v0, v4, v8
	v_lshl_add_u64 v[2:3], v[10:11], 0, v[2:3]
	global_store_dword v[2:3], v0, off
	v_or_b32_e32 v2, 3, v18
	v_ashrrev_i32_e32 v3, 31, v2
	v_lshlrev_b64 v[2:3], 6, v[2:3]
	s_lshl_b32 s98, s45, 2
	s_add_i32 s1, s1, s98
	v_add_f32_e32 v0, v5, v9
	v_lshl_add_u64 v[2:3], v[10:11], 0, v[2:3]
	s_cmpk_gt_i32 s1, 0x3ff
	v_add_u32_e32 v16, s0, v16
	global_store_dword v[2:3], v0, off
	s_cbranch_scc0 .LBB0_313
